# attention: previous tile's softmax tail (exp/row-sum/packs) list-scheduled into the QK MFMA shadows (36 of 74 VALU per tile)
# baseline (speedup 1.0000x reference)
.LBB0_1173:
	s_mul_hi_u32 s7, s80, 0xaaaaaaab
	s_lshr_b32 s7, s7, 1
	s_mul_i32 s7, s7, 0xfffee000
	v_add_u32_e32 v166, s6, v159
	v_add_u32_e32 v167, s6, v161
	v_add_u32_e32 v185, s6, v162
	v_add_u32_e32 v230, s6, v163
	ds_read_b128 v[66:69], v166 offset:32768
	ds_read_b128 v[82:85], v167 offset:32768
	ds_read_b128 v[86:89], v185 offset:32768
	ds_read_b128 v[90:93], v230 offset:32768
	ds_read_b128 v[94:97], v166 offset:32896
	ds_read_b128 v[186:189], v167 offset:32896
	ds_read_b128 v[190:193], v185 offset:32896
	ds_read_b128 v[194:197], v230 offset:32896
	ds_read_b128 v[198:201], v158
	ds_read_b128 v[202:205], v166 offset:33024
	ds_read_b128 v[206:209], v158 offset:1024
	ds_read_b128 v[210:213], v167 offset:33024
	ds_read_b128 v[214:217], v158 offset:2048
	ds_read_b128 v[218:221], v185 offset:33024
	ds_read_b128 v[222:225], v158 offset:3072
	s_waitcnt lgkmcnt(14)
	v_mfma_f32_32x32x16_bf16 v[66:81], v[66:69], v[126:129], 0
	ds_read_b128 v[226:229], v230 offset:33024
	v_exp_f32_e32 v146, v146
	v_exp_f32_e32 v147, v147
	s_waitcnt lgkmcnt(11)
	v_mfma_f32_32x32x16_bf16 v[66:81], v[82:85], v[122:125], v[66:81]
	v_exp_f32_e32 v132, v132
	v_exp_f32_e32 v133, v133
	v_mfma_f32_32x32x16_bf16 v[66:81], v[86:89], v[118:121], v[66:81]
	v_mfma_f32_32x32x16_bf16 v[66:81], v[90:93], v[114:117], v[66:81]
	v_mfma_f32_32x32x16_bf16 v[66:81], v[94:97], v[110:113], v[66:81]
	s_waitcnt lgkmcnt(8)
	v_mfma_f32_32x32x16_bf16 v[66:81], v[186:189], v[106:109], v[66:81]
	ds_read_b128 v[186:189], v166 offset:45056
	v_mfma_f32_32x32x16_bf16 v[66:81], v[190:193], v[102:105], v[66:81]
	ds_read_b128 v[190:193], v167 offset:45056
	v_mfma_f32_32x32x16_bf16 v[66:81], v[194:197], v[98:101], v[66:81]
	ds_read_b128 v[194:197], v185 offset:45056
	s_waitcnt lgkmcnt(3)
	v_mfma_f32_32x32x16_bf16 v[66:81], v[202:205], v[198:201], v[66:81]
	ds_read_b128 v[202:205], v230 offset:45056
	v_mfma_f32_32x32x16_bf16 v[66:81], v[210:213], v[206:209], v[66:81]
	ds_read_b128 v[210:213], v166 offset:45184
	v_mfma_f32_32x32x16_bf16 v[66:81], v[218:221], v[214:217], v[66:81]
	ds_read_b128 v[218:221], v167 offset:45184
	v_mfma_f32_32x32x16_bf16 v[66:81], v[226:229], v[222:225], v[66:81]
	ds_read_b128 v[226:229], v185 offset:45184
	s_waitcnt lgkmcnt(3)
	v_mfma_f32_32x32x16_bf16 v[82:97], v[186:189], v[126:129], 0
	ds_read_b128 v[186:189], v230 offset:45184
	s_add_i32 s6, s78, 1
	s_min_u32 s6, s6, s14
	v_mfma_f32_32x32x16_bf16 v[82:97], v[190:193], v[122:125], v[82:97]
	ds_read_b128 v[246:249], v166 offset:45312
	v_cvt_pk_bf16_f32 v166, v146, v147
	s_lshl_b32 s10, s6, 6
	v_mfma_f32_32x32x16_bf16 v[82:97], v[194:197], v[118:121], v[82:97]
	ds_read_b128 v[242:245], v167 offset:45312
	v_exp_f32_e32 v167, v144
	v_exp_f32_e32 v190, v138
	s_cmp_lt_u32 s6, 4
	s_cselect_b32 s6, s74, s15
	s_add_i32 s6, s6, s10
	v_mfma_f32_32x32x16_bf16 v[82:97], v[202:205], v[114:117], v[82:97]
	ds_read_b128 v[238:241], v185 offset:45312
	v_exp_f32_e32 v194, v130
	v_add_f32_e32 v130, 0, v178
	v_add_f32_e32 v130, v182, v130
	s_mul_hi_i32 s11, s6, 0x1080
	s_mulk_i32 s6, 0x1080
	s_waitcnt lgkmcnt(3)
	v_mfma_f32_32x32x16_bf16 v[82:97], v[210:213], v[110:113], v[82:97]
	ds_read_b128 v[234:237], v230 offset:45312
	v_add_f32_e32 v130, v179, v130
	v_add_f32_e32 v130, v183, v130
	v_add_f32_e32 v130, v180, v130
	v_add_f32_e32 v130, v184, v130
	s_add_u32 s10, s3, s6
	s_addc_u32 s11, s35, s11
	s_add_i32 s6, s7, s30
	v_mfma_f32_32x32x16_bf16 v[82:97], v[218:221], v[106:109], v[82:97]
	v_add_f32_e32 v130, v177, v130
	v_add_f32_e32 v130, v181, v130
	v_add_f32_e32 v130, v171, v130
	v_add_f32_e32 v130, v175, v130
	s_add_i32 s6, s6, s8
	s_add_i32 m0, s6, 0x1a000
	s_nop 0
	global_load_lds_dwordx4 v232, s[10:11]
	v_mfma_f32_32x32x16_bf16 v[82:97], v[226:229], v[102:105], v[82:97]
	v_add_f32_e32 v130, v172, v130
	v_add_f32_e32 v130, v176, v130
	v_add_f32_e32 v130, v168, v130
	v_add_f32_e32 v130, v173, v130
	s_add_i32 m0, s6, 0x1a400
	v_mfma_f32_32x32x16_bf16 v[82:97], v[186:189], v[98:101], v[82:97]
	v_add_f32_e32 v130, v169, v130
	v_exp_f32_e32 v185, v145
	v_add_f32_e32 v130, v174, v130
	global_load_lds_dwordx4 v251, s[10:11]
	s_add_i32 m0, s6, 0x1a800
	s_waitcnt lgkmcnt(0)
	v_mfma_f32_32x32x16_bf16 v[82:97], v[246:249], v[198:201], v[82:97]
	v_exp_f32_e32 v186, v142
	v_add_f32_e32 v130, v146, v130
	v_add_f32_e32 v130, v147, v130
	v_mfma_f32_32x32x16_bf16 v[82:97], v[242:245], v[206:209], v[82:97]
	v_exp_f32_e32 v187, v143
	v_exp_f32_e32 v188, v140
	global_load_lds_dwordx4 v252, s[10:11]
	v_mfma_f32_32x32x16_bf16 v[82:97], v[238:241], v[214:217], v[82:97]
	v_add_f32_e32 v130, v167, v130
	v_exp_f32_e32 v189, v141
	v_add_f32_e32 v130, v185, v130
	v_mfma_f32_32x32x16_bf16 v[82:97], v[234:237], v[222:225], v[82:97]
	v_add_f32_e32 v130, v186, v130
	v_exp_f32_e32 v191, v139
	v_add_f32_e32 v130, v187, v130
	v_exp_f32_e32 v192, v136
	v_add_f32_e32 v130, v188, v130
	v_exp_f32_e32 v193, v137
	v_add_f32_e32 v130, v189, v130
	v_add_f32_e32 v130, v190, v130
	v_add_f32_e32 v130, v191, v130
	v_add_f32_e32 v130, v192, v130
	v_exp_f32_e32 v195, v131
	v_add_f32_e32 v130, v193, v130
	v_add_f32_e32 v130, v132, v130
	v_add_f32_e32 v130, v133, v130
	v_add_f32_e32 v130, v194, v130
	v_add_f32_e32 v136, v195, v130
	v_mov_b32_e32 v137, v136
	v_cvt_pk_bf16_f32 v138, v178, v182
	v_cvt_pk_bf16_f32 v139, v179, v183
	v_cvt_pk_bf16_f32 v140, v180, v184
	v_cvt_pk_bf16_f32 v141, v177, v181
	v_cvt_pk_bf16_f32 v142, v171, v175
	v_cvt_pk_bf16_f32 v143, v172, v176
	v_cvt_pk_bf16_f32 v144, v168, v173
	v_cvt_pk_bf16_f32 v145, v169, v174
	v_cvt_pk_bf16_f32 v167, v167, v185
	v_cvt_pk_bf16_f32 v168, v186, v187
	v_cvt_pk_bf16_f32 v169, v188, v189
	v_permlane32_swap_b32_e32 v136, v137
	v_permlane32_swap_b32_e32 v138, v140
	v_permlane32_swap_b32_e32 v167, v169
	v_cvt_pk_bf16_f32 v130, v190, v191
	v_cvt_pk_bf16_f32 v131, v192, v193
	v_cvt_pk_bf16_f32 v132, v132, v133
	v_cvt_pk_bf16_f32 v133, v194, v195
	v_permlane32_swap_b32_e32 v139, v141
	v_permlane32_swap_b32_e32 v142, v144
	v_permlane32_swap_b32_e32 v143, v145
	v_permlane32_swap_b32_e32 v166, v168
	v_permlane32_swap_b32_e32 v130, v132
	v_permlane32_swap_b32_e32 v131, v133
	ds_read_b64_tr_b16 v[172:173], v160 offset:0
	ds_read_b64_tr_b16 v[174:175], v160 offset:0x800
	ds_read_b64_tr_b16 v[176:177], v160 offset:0x1000
	ds_read_b64_tr_b16 v[178:179], v160 offset:0x1800
	ds_read_b64_tr_b16 v[180:181], v160 offset:0x2000
	ds_read_b64_tr_b16 v[182:183], v160 offset:0x2800
	ds_read_b64_tr_b16 v[184:185], v160 offset:0x3000
	ds_read_b64_tr_b16 v[186:187], v160 offset:0x3800
	s_nop 0
	s_waitcnt lgkmcnt(4)
	v_mfma_f32_32x32x16_bf16 v[2:17], v[138:141], v[172:175], v[2:17]
	ds_read_b64_tr_b16 v[172:173], v160 offset:0x200
	ds_read_b64_tr_b16 v[174:175], v160 offset:0xa00
	v_mfma_f32_32x32x16_bf16 v[2:17], v[142:145], v[176:179], v[2:17]
	ds_read_b64_tr_b16 v[176:177], v160 offset:0x1200
	ds_read_b64_tr_b16 v[178:179], v160 offset:0x1a00
	s_waitcnt lgkmcnt(4)
	v_mfma_f32_32x32x16_bf16 v[2:17], v[166:169], v[180:183], v[2:17]
	ds_read_b64_tr_b16 v[180:181], v160 offset:0x2200
	ds_read_b64_tr_b16 v[182:183], v160 offset:0x2a00
	ds_read_b64_tr_b16 v[188:189], v160 offset:0x3200
	ds_read_b64_tr_b16 v[190:191], v160 offset:0x3a00
	v_mfma_f32_32x32x16_bf16 v[2:17], v[130:133], v[184:187], v[2:17]
	s_waitcnt lgkmcnt(4)
	v_mfma_f32_32x32x16_bf16 v[50:65], v[138:141], v[172:175], v[50:65]
	ds_read_b64_tr_b16 v[172:173], v160 offset:0x400
	ds_read_b64_tr_b16 v[174:175], v160 offset:0xc00
	v_mfma_f32_32x32x16_bf16 v[50:65], v[142:145], v[176:179], v[50:65]
	ds_read_b64_tr_b16 v[176:177], v160 offset:0x1400
	ds_read_b64_tr_b16 v[178:179], v160 offset:0x1c00
	s_waitcnt lgkmcnt(4)
	v_mfma_f32_32x32x16_bf16 v[50:65], v[166:169], v[180:183], v[50:65]
	ds_read_b64_tr_b16 v[180:181], v160 offset:0x2400
	ds_read_b64_tr_b16 v[182:183], v160 offset:0x2c00
	ds_read_b64_tr_b16 v[184:185], v160 offset:0x3400
	ds_read_b64_tr_b16 v[186:187], v160 offset:0x3c00
	v_mfma_f32_32x32x16_bf16 v[50:65], v[130:133], v[188:191], v[50:65]
	s_waitcnt lgkmcnt(4)
	v_mfma_f32_32x32x16_bf16 v[34:49], v[138:141], v[172:175], v[34:49]
	ds_read_b64_tr_b16 v[172:173], v160 offset:0x600
	ds_read_b64_tr_b16 v[174:175], v160 offset:0xe00
	v_mfma_f32_32x32x16_bf16 v[34:49], v[142:145], v[176:179], v[34:49]
	ds_read_b64_tr_b16 v[176:177], v160 offset:0x1600
	ds_read_b64_tr_b16 v[178:179], v160 offset:0x1e00
	s_waitcnt lgkmcnt(4)
	v_mfma_f32_32x32x16_bf16 v[34:49], v[166:169], v[180:183], v[34:49]
	ds_read_b64_tr_b16 v[180:181], v160 offset:0x2600
	ds_read_b64_tr_b16 v[182:183], v160 offset:0x2e00
	ds_read_b64_tr_b16 v[188:189], v160 offset:0x3600
	ds_read_b64_tr_b16 v[190:191], v160 offset:0x3e00
	v_mfma_f32_32x32x16_bf16 v[34:49], v[130:133], v[184:187], v[34:49]
	v_max_f32_e32 v146, v67, v67
	v_max_f32_e32 v147, v66, v66
	v_max_f32_e32 v146, v147, v146
	v_max3_f32 v146, v146, v68, v69
	v_max3_f32 v146, v146, v70, v71
	s_waitcnt lgkmcnt(4)
	v_mfma_f32_32x32x16_bf16 v[18:33], v[138:141], v[172:175], v[18:33]
	v_max3_f32 v138, v146, v72, v73
	v_max3_f32 v138, v138, v74, v75
	v_max3_f32 v138, v138, v76, v77
	v_max3_f32 v138, v138, v78, v79
	v_max3_f32 v138, v138, v80, v81
	v_max3_f32 v138, v138, v82, v83
	v_max3_f32 v138, v138, v84, v85
	v_max3_f32 v138, v138, v86, v87
	v_max3_f32 v138, v138, v88, v89
	v_max3_f32 v138, v138, v90, v91
	v_max3_f32 v138, v138, v92, v93
	v_max3_f32 v138, v138, v94, v95
	v_max3_f32 v138, v138, v96, v97
	v_mov_b32_e32 v139, v138
	s_nop 1
	v_permlane32_swap_b32_e32 v138, v139
	v_max_f32_e32 v139, v139, v139
	v_max_f32_e32 v138, v138, v138
	v_max_f32_e32 v138, v138, v139
	v_sub_f32_e32 v139, v138, v165
	v_mfma_f32_32x32x16_bf16 v[18:33], v[142:145], v[176:179], v[18:33]
	v_cmp_ge_f32_e32 vcc, s65, v139
	s_waitcnt vmcnt(3) lgkmcnt(0)
	s_barrier
	s_cmp_eq_u64 vcc, exec
	s_cselect_b64 s[6:7], -1, 0
	s_cmp_lt_u32 s78, 4
	s_cselect_b32 s12, s74, s15
	s_add_i32 s12, s12, s9
	s_mul_hi_i32 s13, s12, 0x1080
	s_mulk_i32 s12, 0x1080
	s_add_u32 s12, s3, s12
	s_mov_b32 m0, s70
	s_addc_u32 s13, s35, s13
	global_load_lds_dwordx4 v253, s[12:13]
	s_mov_b32 m0, s72
	v_mfma_f32_32x32x16_bf16 v[18:33], v[166:169], v[180:183], v[18:33]
	global_load_lds_dwordx4 v254, s[12:13]
	v_max_f32_e32 v139, v165, v165
	v_max_f32_e32 v138, v139, v138
	v_sub_f32_e32 v139, v165, v138
	v_mul_f32_e32 v139, 0x3dd53b94, v139
	v_exp_f32_e32 v139, v139
	v_mfma_f32_32x32x16_bf16 v[18:33], v[130:133], v[188:191], v[18:33]
	v_cndmask_b32_e64 v167, v139, 1.0, s[6:7]
	v_cmp_gt_f32_e32 vcc, 1.0, v167
	s_cbranch_vccz .LBB0_1177
	s_and_saveexec_b64 s[12:13], s[4:5]
	ds_write_b32 v155, v167 offset:128
	s_or_b64 exec, exec, s[12:13]
	s_waitcnt lgkmcnt(0)
	v_add_u32_e32 v139, s69, v134
	ds_read_b128 v[130:133], v139 offset:224
	ds_read_b128 v[140:143], v139 offset:192
	ds_read_b128 v[144:147], v139 offset:160
	ds_read_b128 v[172:175], v139 offset:128
	s_waitcnt lgkmcnt(0)
	v_pk_mul_f32 v[14:15], v[14:15], v[130:131]
	v_pk_mul_f32 v[10:11], v[10:11], v[140:141]
	v_pk_mul_f32 v[6:7], v[6:7], v[144:145]
	v_pk_mul_f32 v[16:17], v[16:17], v[132:133]
	v_pk_mul_f32 v[12:13], v[12:13], v[142:143]
	v_pk_mul_f32 v[8:9], v[8:9], v[146:147]
	v_pk_mul_f32 v[4:5], v[4:5], v[174:175]
	v_pk_mul_f32 v[2:3], v[2:3], v[172:173]
	v_pk_mul_f32 v[62:63], v[62:63], v[130:131]
	v_pk_mul_f32 v[58:59], v[58:59], v[140:141]
	v_pk_mul_f32 v[54:55], v[54:55], v[144:145]
	v_pk_mul_f32 v[64:65], v[64:65], v[132:133]
	v_pk_mul_f32 v[60:61], v[60:61], v[142:143]
	v_pk_mul_f32 v[56:57], v[56:57], v[146:147]
	v_pk_mul_f32 v[52:53], v[52:53], v[174:175]
	v_pk_mul_f32 v[50:51], v[50:51], v[172:173]
	v_pk_mul_f32 v[46:47], v[46:47], v[130:131]
	v_pk_mul_f32 v[42:43], v[42:43], v[140:141]
	v_pk_mul_f32 v[38:39], v[38:39], v[144:145]
	v_pk_mul_f32 v[48:49], v[48:49], v[132:133]
	v_pk_mul_f32 v[44:45], v[44:45], v[142:143]
	v_pk_mul_f32 v[40:41], v[40:41], v[146:147]
	v_pk_mul_f32 v[36:37], v[36:37], v[174:175]
	v_pk_mul_f32 v[34:35], v[34:35], v[172:173]
	v_pk_mul_f32 v[30:31], v[30:31], v[130:131]
	v_pk_mul_f32 v[26:27], v[26:27], v[140:141]
	v_pk_mul_f32 v[22:23], v[22:23], v[144:145]
	v_pk_mul_f32 v[32:33], v[32:33], v[132:133]
	v_pk_mul_f32 v[28:29], v[28:29], v[142:143]
	v_pk_mul_f32 v[24:25], v[24:25], v[146:147]
	v_pk_mul_f32 v[20:21], v[20:21], v[174:175]
	v_pk_mul_f32 v[18:19], v[18:19], v[172:173]
.LBB0_1177:
	v_cndmask_b32_e64 v130, v138, v165, s[6:7]
	s_mul_hi_u32 s12, s79, 0xaaaaaaab
	v_mul_f32_e32 v131, 0xbdd53b94, v130
	s_lshr_b32 s12, s12, 1
	v_fmamk_f32 v66, v66, 0x3dd53b94, v131
	v_fmamk_f32 v68, v68, 0x3dd53b94, v131
	v_fmamk_f32 v70, v70, 0x3dd53b94, v131
	v_fmamk_f32 v72, v72, 0x3dd53b94, v131
	s_mul_i32 s12, s12, 0xfffee000
	v_fmamk_f32 v74, v74, 0x3dd53b94, v131
	v_fmamk_f32 v76, v76, 0x3dd53b94, v131
	v_fmamk_f32 v78, v78, 0x3dd53b94, v131
	v_fmamk_f32 v80, v80, 0x3dd53b94, v131
	v_fmamk_f32 v132, v82, 0x3dd53b94, v131
	v_fmamk_f32 v133, v84, 0x3dd53b94, v131
	v_fmamk_f32 v146, v86, 0x3dd53b94, v131
	v_fmamk_f32 v147, v88, 0x3dd53b94, v131
	v_fmamk_f32 v165, v90, 0x3dd53b94, v131
	v_fmamk_f32 v166, v92, 0x3dd53b94, v131
	v_fmamk_f32 v168, v94, 0x3dd53b94, v131
	v_fmamk_f32 v169, v96, 0x3dd53b94, v131
	v_exp_f32_e32 v171, v66
	v_exp_f32_e32 v224, v68
	v_exp_f32_e32 v225, v70
	v_exp_f32_e32 v226, v72
	v_fmamk_f32 v66, v67, 0x3dd53b94, v131
	v_fmamk_f32 v67, v69, 0x3dd53b94, v131
	v_fmamk_f32 v68, v71, 0x3dd53b94, v131
	v_fmamk_f32 v69, v73, 0x3dd53b94, v131
	v_fmamk_f32 v70, v75, 0x3dd53b94, v131
	v_fmamk_f32 v71, v77, 0x3dd53b94, v131
	v_fmamk_f32 v72, v79, 0x3dd53b94, v131
	v_fmamk_f32 v73, v81, 0x3dd53b94, v131
	v_fmamk_f32 v231, v83, 0x3dd53b94, v131
	v_fmamk_f32 v233, v85, 0x3dd53b94, v131
	v_fmamk_f32 v234, v87, 0x3dd53b94, v131
	v_fmamk_f32 v235, v89, 0x3dd53b94, v131
	v_fmamk_f32 v236, v91, 0x3dd53b94, v131
	v_fmamk_f32 v245, v93, 0x3dd53b94, v131
	v_fmamk_f32 v246, v95, 0x3dd53b94, v131
	v_fmac_f32_e32 v131, 0x3dd53b94, v97
	v_exp_f32_e32 v227, v74
	v_exp_f32_e32 v228, v76
	v_exp_f32_e32 v229, v78
	v_exp_f32_e32 v230, v80
	v_exp_f32_e32 v237, v66
	v_exp_f32_e32 v238, v67
	v_exp_f32_e32 v239, v68
	v_exp_f32_e32 v240, v69
	v_exp_f32_e32 v241, v70
	v_exp_f32_e32 v242, v71
	v_exp_f32_e32 v243, v72
	v_exp_f32_e32 v244, v73
	v_add_u32_e32 v196, s16, v159
	v_add_u32_e32 v204, s16, v161
	v_add_u32_e32 v212, s16, v162
	v_add_u32_e32 v220, s16, v163
	ds_read_b128 v[66:69], v196 offset:32768
	ds_read_b128 v[82:85], v204 offset:32768
	ds_read_b128 v[86:89], v212 offset:32768
	ds_read_b128 v[90:93], v220 offset:32768
	ds_read_b128 v[94:97], v196 offset:32896
	ds_read_b128 v[138:141], v204 offset:32896
	ds_read_b128 v[142:145], v212 offset:32896
	ds_read_b128 v[172:175], v220 offset:32896
	ds_read_b128 v[176:179], v158
	ds_read_b128 v[180:183], v196 offset:33024
	ds_read_b128 v[184:187], v158 offset:1024
	ds_read_b128 v[188:191], v204 offset:33024
	ds_read_b128 v[192:195], v158 offset:2048
	ds_read_b128 v[200:203], v212 offset:33024
	ds_read_b128 v[208:211], v158 offset:3072
	s_waitcnt lgkmcnt(14)
	v_mfma_f32_32x32x16_bf16 v[66:81], v[66:69], v[126:129], 0
	ds_read_b128 v[216:219], v220 offset:33024
	v_exp_f32_e32 v132, v132
	v_exp_f32_e32 v133, v133
	s_waitcnt lgkmcnt(11)
	v_mfma_f32_32x32x16_bf16 v[66:81], v[82:85], v[122:125], v[66:81]
	v_exp_f32_e32 v146, v146
	v_exp_f32_e32 v147, v147
	v_mfma_f32_32x32x16_bf16 v[66:81], v[86:89], v[118:121], v[66:81]
	v_exp_f32_e32 v165, v165
	v_exp_f32_e32 v166, v166
	v_mfma_f32_32x32x16_bf16 v[66:81], v[90:93], v[114:117], v[66:81]
	v_exp_f32_e32 v168, v168
	v_exp_f32_e32 v169, v169
	v_mfma_f32_32x32x16_bf16 v[66:81], v[94:97], v[110:113], v[66:81]
	v_exp_f32_e32 v131, v131
	s_waitcnt lgkmcnt(8)
	v_mfma_f32_32x32x16_bf16 v[66:81], v[138:141], v[106:109], v[66:81]
	ds_read_b128 v[138:141], v196 offset:45056
	v_mfma_f32_32x32x16_bf16 v[66:81], v[142:145], v[102:105], v[66:81]
	ds_read_b128 v[142:145], v204 offset:45056
	v_mfma_f32_32x32x16_bf16 v[66:81], v[172:175], v[98:101], v[66:81]
	ds_read_b128 v[172:175], v212 offset:45056
	s_waitcnt lgkmcnt(3)
	v_mfma_f32_32x32x16_bf16 v[66:81], v[180:183], v[176:179], v[66:81]
	ds_read_b128 v[180:183], v220 offset:45056
	v_mfma_f32_32x32x16_bf16 v[66:81], v[188:191], v[184:187], v[66:81]
	ds_read_b128 v[188:191], v196 offset:45184
	v_mfma_f32_32x32x16_bf16 v[66:81], v[200:203], v[192:195], v[66:81]
	ds_read_b128 v[200:203], v204 offset:45184
	v_mfma_f32_32x32x16_bf16 v[66:81], v[216:219], v[208:211], v[66:81]
	ds_read_b128 v[216:219], v212 offset:45184
	s_waitcnt lgkmcnt(3)
	v_mfma_f32_32x32x16_bf16 v[82:97], v[138:141], v[126:129], 0
	ds_read_b128 v[138:141], v220 offset:45184
	s_add_i32 s78, s78, 2
	s_min_u32 s6, s78, s14
	s_lshl_b32 s7, s6, 6
	s_cmp_lt_u32 s6, 4
	s_cselect_b32 s6, s74, s15
	s_add_i32 s6, s6, s7
	s_mul_hi_i32 s7, s6, 0x1080
	v_mfma_f32_32x32x16_bf16 v[82:97], v[142:145], v[122:125], v[82:97]
	ds_read_b128 v[196:199], v196 offset:45312
	s_mulk_i32 s6, 0x1080
	v_mfma_f32_32x32x16_bf16 v[82:97], v[172:175], v[118:121], v[82:97]
	ds_read_b128 v[204:207], v204 offset:45312
	v_cvt_pk_bf16_f32 v142, v227, v241
	v_cvt_pk_bf16_f32 v143, v228, v242
	v_cvt_pk_bf16_f32 v144, v229, v243
	v_cvt_pk_bf16_f32 v145, v230, v244
	v_mfma_f32_32x32x16_bf16 v[82:97], v[180:183], v[114:117], v[82:97]
	ds_read_b128 v[212:215], v212 offset:45312
	v_exp_f32_e32 v172, v231
	v_exp_f32_e32 v173, v233
	s_waitcnt lgkmcnt(3)
	v_mfma_f32_32x32x16_bf16 v[82:97], v[188:191], v[110:113], v[82:97]
	ds_read_b128 v[220:223], v220 offset:45312
	v_exp_f32_e32 v174, v234
	v_exp_f32_e32 v175, v235
	s_add_u32 s6, s3, s6
	s_addc_u32 s7, s35, s7
	s_add_i32 s12, s12, s30
	v_mfma_f32_32x32x16_bf16 v[82:97], v[200:203], v[106:109], v[82:97]
	v_permlane32_swap_b32_e32 v142, v144
	v_permlane32_swap_b32_e32 v143, v145
	s_add_i32 s12, s12, s8
	s_add_i32 m0, s12, 0x20000
	s_nop 0
	global_load_lds_dwordx4 v232, s[6:7]
	v_mfma_f32_32x32x16_bf16 v[82:97], v[216:219], v[102:105], v[82:97]
	s_add_i32 m0, s12, 0x20400
	v_mfma_f32_32x32x16_bf16 v[82:97], v[138:141], v[98:101], v[82:97]
	global_load_lds_dwordx4 v251, s[6:7]
	s_add_i32 m0, s12, 0x20800
	s_waitcnt lgkmcnt(0)
	v_mfma_f32_32x32x16_bf16 v[82:97], v[196:199], v[176:179], v[82:97]
	v_add_f32_e32 v138, 0, v171
	v_add_f32_e32 v138, v237, v138
	v_add_f32_e32 v138, v224, v138
	v_add_f32_e32 v138, v238, v138
	v_mfma_f32_32x32x16_bf16 v[82:97], v[204:207], v[184:187], v[82:97]
	v_add_f32_e32 v138, v225, v138
	v_add_f32_e32 v138, v239, v138
	v_add_f32_e32 v138, v226, v138
	v_add_f32_e32 v138, v240, v138
	global_load_lds_dwordx4 v252, s[6:7]
	v_mfma_f32_32x32x16_bf16 v[82:97], v[212:215], v[192:195], v[82:97]
	v_add_f32_e32 v138, v227, v138
	v_add_f32_e32 v138, v241, v138
	v_add_f32_e32 v138, v228, v138
	v_add_f32_e32 v138, v242, v138
	v_mfma_f32_32x32x16_bf16 v[82:97], v[220:223], v[208:211], v[82:97]
	v_add_f32_e32 v138, v229, v138
	v_add_f32_e32 v138, v243, v138
	v_add_f32_e32 v138, v230, v138
	v_add_f32_e32 v138, v244, v138
	v_add_f32_e32 v138, v132, v138
	v_add_f32_e32 v138, v172, v138
	v_add_f32_e32 v138, v133, v138
	v_add_f32_e32 v138, v173, v138
	v_add_f32_e32 v138, v146, v138
	v_exp_f32_e32 v176, v236
	v_add_f32_e32 v138, v174, v138
	v_add_f32_e32 v138, v147, v138
	v_exp_f32_e32 v177, v245
	v_add_f32_e32 v138, v175, v138
	v_add_f32_e32 v138, v165, v138
	v_exp_f32_e32 v178, v246
	v_add_f32_e32 v138, v176, v138
	v_add_f32_e32 v138, v166, v138
	v_add_f32_e32 v138, v177, v138
	v_add_f32_e32 v138, v168, v138
	v_add_f32_e32 v138, v178, v138
	v_add_f32_e32 v138, v169, v138
	v_add_f32_e32 v185, v131, v138
	v_mov_b32_e32 v186, v185
	s_nop 0
	s_nop 0
	v_permlane32_swap_b32_e32 v185, v186
	v_cvt_pk_bf16_f32 v138, v171, v237
	v_cvt_pk_bf16_f32 v139, v224, v238
	v_cvt_pk_bf16_f32 v140, v225, v239
	v_cvt_pk_bf16_f32 v141, v226, v240
	v_cvt_pk_bf16_f32 v172, v132, v172
	v_cvt_pk_bf16_f32 v173, v133, v173
	v_cvt_pk_bf16_f32 v174, v146, v174
	v_cvt_pk_bf16_f32 v175, v147, v175
	v_cvt_pk_bf16_f32 v176, v165, v176
	v_cvt_pk_bf16_f32 v177, v166, v177
	v_cvt_pk_bf16_f32 v178, v168, v178
	v_cvt_pk_bf16_f32 v179, v169, v131
	v_permlane32_swap_b32_e32 v138, v140
	v_permlane32_swap_b32_e32 v139, v141
	v_permlane32_swap_b32_e32 v172, v174
	v_permlane32_swap_b32_e32 v173, v175
	v_permlane32_swap_b32_e32 v176, v178
	v_permlane32_swap_b32_e32 v177, v179
	ds_read_b64_tr_b16 v[180:181], v156 offset:0
	ds_read_b64_tr_b16 v[182:183], v156 offset:0x800
	ds_read_b64_tr_b16 v[188:189], v156 offset:0x1000
	ds_read_b64_tr_b16 v[190:191], v156 offset:0x1800
	ds_read_b64_tr_b16 v[192:193], v156 offset:0x2000
	ds_read_b64_tr_b16 v[194:195], v156 offset:0x2800
	ds_read_b64_tr_b16 v[196:197], v156 offset:0x3000
	ds_read_b64_tr_b16 v[198:199], v156 offset:0x3800
	s_nop 0
	s_waitcnt lgkmcnt(4)
	v_mfma_f32_32x32x16_bf16 v[2:17], v[138:141], v[180:183], v[2:17]
	ds_read_b64_tr_b16 v[180:181], v156 offset:0x200
	ds_read_b64_tr_b16 v[182:183], v156 offset:0xa00
	v_mfma_f32_32x32x16_bf16 v[2:17], v[142:145], v[188:191], v[2:17]
	ds_read_b64_tr_b16 v[188:189], v156 offset:0x1200
	ds_read_b64_tr_b16 v[190:191], v156 offset:0x1a00
	s_waitcnt lgkmcnt(4)
	v_mfma_f32_32x32x16_bf16 v[2:17], v[172:175], v[192:195], v[2:17]
	ds_read_b64_tr_b16 v[192:193], v156 offset:0x2200
	ds_read_b64_tr_b16 v[194:195], v156 offset:0x2a00
	ds_read_b64_tr_b16 v[200:201], v156 offset:0x3200
	ds_read_b64_tr_b16 v[202:203], v156 offset:0x3a00
	v_mfma_f32_32x32x16_bf16 v[2:17], v[176:179], v[196:199], v[2:17]
	s_waitcnt lgkmcnt(4)
	v_mfma_f32_32x32x16_bf16 v[50:65], v[138:141], v[180:183], v[50:65]
	ds_read_b64_tr_b16 v[180:181], v156 offset:0x400
	ds_read_b64_tr_b16 v[182:183], v156 offset:0xc00
	v_mfma_f32_32x32x16_bf16 v[50:65], v[142:145], v[188:191], v[50:65]
	ds_read_b64_tr_b16 v[188:189], v156 offset:0x1400
	ds_read_b64_tr_b16 v[190:191], v156 offset:0x1c00
	s_waitcnt lgkmcnt(4)
	v_mfma_f32_32x32x16_bf16 v[50:65], v[172:175], v[192:195], v[50:65]
	ds_read_b64_tr_b16 v[192:193], v156 offset:0x2400
	ds_read_b64_tr_b16 v[194:195], v156 offset:0x2c00
	ds_read_b64_tr_b16 v[196:197], v156 offset:0x3400
	ds_read_b64_tr_b16 v[198:199], v156 offset:0x3c00
	v_mfma_f32_32x32x16_bf16 v[50:65], v[176:179], v[200:203], v[50:65]
	s_waitcnt lgkmcnt(4)
	v_mfma_f32_32x32x16_bf16 v[34:49], v[138:141], v[180:183], v[34:49]
	ds_read_b64_tr_b16 v[180:181], v156 offset:0x600
	ds_read_b64_tr_b16 v[182:183], v156 offset:0xe00
	v_mfma_f32_32x32x16_bf16 v[34:49], v[142:145], v[188:191], v[34:49]
	ds_read_b64_tr_b16 v[188:189], v156 offset:0x1600
	ds_read_b64_tr_b16 v[190:191], v156 offset:0x1e00
	s_waitcnt lgkmcnt(4)
	v_mfma_f32_32x32x16_bf16 v[34:49], v[172:175], v[192:195], v[34:49]
	ds_read_b64_tr_b16 v[192:193], v156 offset:0x2600
	ds_read_b64_tr_b16 v[194:195], v156 offset:0x2e00
	ds_read_b64_tr_b16 v[200:201], v156 offset:0x3600
	ds_read_b64_tr_b16 v[202:203], v156 offset:0x3e00
	v_mfma_f32_32x32x16_bf16 v[34:49], v[176:179], v[196:199], v[34:49]
	s_waitcnt vmcnt(3) lgkmcnt(0)
	s_barrier
	v_mfma_f32_32x32x16_bf16 v[18:33], v[138:141], v[180:183], v[18:33]
	s_mov_b32 m0, s76
	s_nop 0
	global_load_lds_dwordx4 v253, s[10:11]
	s_mov_b32 m0, s77
	v_max_f32_e32 v132, v66, v66
	global_load_lds_dwordx4 v254, s[10:11]
	v_max_f32_e32 v131, v67, v67
	v_max_f32_e32 v131, v132, v131
	v_max3_f32 v131, v131, v68, v69
	v_max3_f32 v131, v131, v70, v71
	v_max3_f32 v131, v131, v72, v73
	v_max3_f32 v131, v131, v74, v75
	v_mfma_f32_32x32x16_bf16 v[18:33], v[142:145], v[188:191], v[18:33]
	v_max3_f32 v131, v131, v76, v77
	v_max3_f32 v131, v131, v78, v79
	v_max3_f32 v131, v131, v80, v81
	v_max3_f32 v131, v131, v82, v83
	v_max3_f32 v131, v131, v84, v85
	v_max3_f32 v131, v131, v86, v87
	v_max3_f32 v131, v131, v88, v89
	v_max3_f32 v131, v131, v90, v91
	v_mfma_f32_32x32x16_bf16 v[18:33], v[172:175], v[192:195], v[18:33]
	v_max3_f32 v131, v131, v92, v93
	v_max3_f32 v131, v131, v94, v95
	v_max3_f32 v131, v131, v96, v97
	v_mov_b32_e32 v132, v131
	s_nop 1
	v_permlane32_swap_b32_e32 v131, v132
	v_max_f32_e32 v132, v132, v132
	v_max_f32_e32 v131, v131, v131
	v_max_f32_e32 v131, v131, v132
	v_max_f32_e32 v133, v130, v130
	v_sub_f32_e32 v132, v131, v130
	v_max_f32_e32 v131, v133, v131
	v_mfma_f32_32x32x16_bf16 v[18:33], v[176:179], v[200:203], v[18:33]
	v_sub_f32_e32 v133, v130, v131
	v_mul_f32_e32 v133, 0x3dd53b94, v133
	v_exp_f32_e32 v133, v133
	v_cmp_ge_f32_e32 vcc, s65, v132
	s_cmp_eq_u64 vcc, exec
	s_cselect_b64 s[6:7], -1, 0
	v_cndmask_b32_e64 v166, v133, 1.0, s[6:7]
	v_cmp_gt_f32_e32 vcc, 1.0, v166
	s_cbranch_vccz .LBB0_1181
	s_and_saveexec_b64 s[10:11], s[4:5]
	ds_write_b32 v155, v166 offset:128
	s_or_b64 exec, exec, s[10:11]
	s_waitcnt lgkmcnt(0)
	v_add_u32_e32 v132, s69, v134
	ds_read_b128 v[138:141], v132 offset:224
	ds_read_b128 v[142:145], v132 offset:192
	ds_read_b128 v[172:175], v132 offset:160
	ds_read_b128 v[176:179], v132 offset:128
	s_waitcnt lgkmcnt(0)
	v_pk_mul_f32 v[14:15], v[14:15], v[138:139]
	v_pk_mul_f32 v[10:11], v[10:11], v[142:143]
	v_pk_mul_f32 v[6:7], v[6:7], v[172:173]
	v_pk_mul_f32 v[16:17], v[16:17], v[140:141]
	v_pk_mul_f32 v[12:13], v[12:13], v[144:145]
	v_pk_mul_f32 v[8:9], v[8:9], v[174:175]
	v_pk_mul_f32 v[4:5], v[4:5], v[178:179]
	v_pk_mul_f32 v[2:3], v[2:3], v[176:177]
	v_pk_mul_f32 v[62:63], v[62:63], v[138:139]
	v_pk_mul_f32 v[58:59], v[58:59], v[142:143]
	v_pk_mul_f32 v[54:55], v[54:55], v[172:173]
	v_pk_mul_f32 v[64:65], v[64:65], v[140:141]
	v_pk_mul_f32 v[60:61], v[60:61], v[144:145]
	v_pk_mul_f32 v[56:57], v[56:57], v[174:175]
	v_pk_mul_f32 v[52:53], v[52:53], v[178:179]
	v_pk_mul_f32 v[50:51], v[50:51], v[176:177]
	v_pk_mul_f32 v[46:47], v[46:47], v[138:139]
	v_pk_mul_f32 v[42:43], v[42:43], v[142:143]
	v_pk_mul_f32 v[38:39], v[38:39], v[172:173]
	v_pk_mul_f32 v[48:49], v[48:49], v[140:141]
	v_pk_mul_f32 v[44:45], v[44:45], v[144:145]
	v_pk_mul_f32 v[40:41], v[40:41], v[174:175]
	v_pk_mul_f32 v[36:37], v[36:37], v[178:179]
	v_pk_mul_f32 v[34:35], v[34:35], v[176:177]
	v_pk_mul_f32 v[30:31], v[30:31], v[138:139]
	v_pk_mul_f32 v[26:27], v[26:27], v[142:143]
	v_pk_mul_f32 v[22:23], v[22:23], v[172:173]
	v_pk_mul_f32 v[32:33], v[32:33], v[140:141]
	v_pk_mul_f32 v[28:29], v[28:29], v[144:145]
	v_pk_mul_f32 v[24:25], v[24:25], v[174:175]
	v_pk_mul_f32 v[20:21], v[20:21], v[178:179]
	v_pk_mul_f32 v[18:19], v[18:19], v[176:177]
